# grid barrier: every workgroup writes back its L2 before arriving (instead of only the last arriver of each XCD after arriving), so the last write-back finds little dirty data
# baseline (speedup 1.0000x reference)
.LBB0_237:
	s_mov_b64 s[6:7], exec
	v_mbcnt_lo_u32_b32 v3, s6, 0
	v_mbcnt_hi_u32_b32 v3, s7, v3
	v_cmp_eq_u32_e32 vcc, 0, v3
	s_and_saveexec_b64 s[2:3], vcc
	s_cbranch_execz .LBB0_239
	v_readlane_b32 s8, v255, 11
	s_lshl_b32 s8, s8, 8
	v_readlane_b32 s10, v255, 9
	v_readlane_b32 s11, v255, 10
	s_add_u32 s8, s10, s8
	s_addc_u32 s9, s11, 0
	s_bcnt1_i32_b64 s6, s[6:7]
	buffer_wbl2 sc1
	s_waitcnt vmcnt(0)
	v_mov_b32_e32 v5, 0x1000
	v_mov_b32_e32 v6, s6
	global_atomic_add v5, v5, v6, s[8:9] offset:1024 sc0

.LBB0_253:
	s_andn2_saveexec_b64 s[2:3], s[2:3]
	s_cbranch_execz .LBB0_271
	s_mov_b64 s[2:3], exec
	s_waitcnt lgkmcnt(0)
	s_waitcnt vmcnt(0)
	v_mbcnt_lo_u32_b32 v3, s2, 0
	v_mbcnt_hi_u32_b32 v3, s3, v3
	v_cmp_eq_u32_e32 vcc, 0, v3
	s_and_saveexec_b64 s[6:7], vcc
	s_cbranch_execz .LBB0_256
	s_bcnt1_i32_b64 s2, s[2:3]
	v_mov_b32_e32 v5, s2
	v_readlane_b32 s2, v255, 9
	v_mov_b32_e32 v4, 0x3000
	v_readlane_b32 s3, v255, 10
	s_nop 4
	global_atomic_add v4, v4, v5, s[2:3] offset:1024 sc0

.LBB0_836:
	s_mov_b64 s[16:17], exec
	v_mbcnt_lo_u32_b32 v3, s16, 0
	v_mbcnt_hi_u32_b32 v3, s17, v3
	v_cmp_eq_u32_e32 vcc, 0, v3
	s_and_saveexec_b64 s[6:7], vcc
	s_cbranch_execz .LBB0_838
	v_readlane_b32 s8, v255, 11
	s_lshl_b32 s8, s8, 8
	v_readlane_b32 s10, v255, 9
	v_readlane_b32 s11, v255, 10
	s_add_u32 s8, s10, s8
	s_addc_u32 s9, s11, 0
	s_bcnt1_i32_b64 s10, s[16:17]
	buffer_wbl2 sc1
	s_waitcnt vmcnt(0)
	v_mov_b32_e32 v5, 0x1000
	v_mov_b32_e32 v6, s10
	global_atomic_add v5, v5, v6, s[8:9] offset:1024 sc0

.LBB0_852:
	s_andn2_saveexec_b64 s[6:7], s[6:7]
	s_cbranch_execz .LBB0_870
	s_mov_b64 s[6:7], exec
	s_waitcnt lgkmcnt(0)
	s_waitcnt vmcnt(0)
	v_mbcnt_lo_u32_b32 v3, s6, 0
	v_mbcnt_hi_u32_b32 v3, s7, v3
	v_cmp_eq_u32_e32 vcc, 0, v3
	s_and_saveexec_b64 s[16:17], vcc
	s_cbranch_execz .LBB0_855
	s_bcnt1_i32_b64 s6, s[6:7]
	v_mov_b32_e32 v5, s6
	v_readlane_b32 s6, v255, 9
	v_mov_b32_e32 v4, 0x3000
	v_readlane_b32 s7, v255, 10
	s_nop 4
	global_atomic_add v4, v4, v5, s[6:7] offset:1024 sc0

.LBB0_916:
	s_mov_b64 s[8:9], exec
	v_mbcnt_lo_u32_b32 v3, s8, 0
	v_mbcnt_hi_u32_b32 v3, s9, v3
	v_cmp_eq_u32_e32 vcc, 0, v3
	s_and_saveexec_b64 s[6:7], vcc
	s_cbranch_execz .LBB0_918
	v_readlane_b32 s10, v255, 11
	s_lshl_b32 s10, s10, 8
	v_readlane_b32 s14, v255, 9
	v_readlane_b32 s15, v255, 10
	s_add_u32 s10, s14, s10
	s_addc_u32 s11, s15, 0
	s_bcnt1_i32_b64 s8, s[8:9]
	buffer_wbl2 sc1
	s_waitcnt vmcnt(0)
	v_mov_b32_e32 v5, 0x1000
	v_mov_b32_e32 v6, s8
	global_atomic_add v5, v5, v6, s[10:11] offset:1024 sc0

.LBB0_932:
	s_andn2_saveexec_b64 s[6:7], s[6:7]
	s_cbranch_execz .LBB0_950
	s_mov_b64 s[6:7], exec
	s_waitcnt lgkmcnt(0)
	s_waitcnt vmcnt(0)
	v_mbcnt_lo_u32_b32 v3, s6, 0
	v_mbcnt_hi_u32_b32 v3, s7, v3
	v_cmp_eq_u32_e32 vcc, 0, v3
	s_and_saveexec_b64 s[8:9], vcc
	s_cbranch_execz .LBB0_935
	s_bcnt1_i32_b64 s6, s[6:7]
	v_mov_b32_e32 v5, s6
	v_readlane_b32 s6, v255, 9
	v_mov_b32_e32 v4, 0x3000
	v_readlane_b32 s7, v255, 10
	s_nop 4
	global_atomic_add v4, v4, v5, s[6:7] offset:1024 sc0

.LBB0_996:
	s_mov_b64 s[8:9], exec
	v_mbcnt_lo_u32_b32 v67, s8, 0
	v_mbcnt_hi_u32_b32 v67, s9, v67
	v_cmp_eq_u32_e32 vcc, 0, v67
	s_and_saveexec_b64 s[6:7], vcc
	s_cbranch_execz .LBB0_998
	v_readlane_b32 s10, v255, 11
	s_lshl_b32 s10, s10, 8
	v_readlane_b32 s12, v255, 9
	v_readlane_b32 s13, v255, 10
	s_add_u32 s10, s12, s10
	s_addc_u32 s11, s13, 0
	s_bcnt1_i32_b64 s8, s[8:9]
	buffer_wbl2 sc1
	s_waitcnt vmcnt(0)
	v_mov_b32_e32 v69, 0x1000
	v_mov_b32_e32 v70, s8
	global_atomic_add v69, v69, v70, s[10:11] offset:1024 sc0

.LBB0_1012:
	s_andn2_saveexec_b64 s[6:7], s[6:7]
	s_cbranch_execz .LBB0_1030
	s_mov_b64 s[6:7], exec
	s_waitcnt lgkmcnt(0)
	s_waitcnt vmcnt(0)
	v_mbcnt_lo_u32_b32 v67, s6, 0
	v_mbcnt_hi_u32_b32 v67, s7, v67
	v_cmp_eq_u32_e32 vcc, 0, v67
	s_and_saveexec_b64 s[8:9], vcc
	s_cbranch_execz .LBB0_1015
	s_bcnt1_i32_b64 s6, s[6:7]
	v_mov_b32_e32 v69, s6
	v_readlane_b32 s6, v255, 9
	v_mov_b32_e32 v68, 0x3000
	v_readlane_b32 s7, v255, 10
	s_nop 4
	global_atomic_add v68, v68, v69, s[6:7] offset:1024 sc0

.LBB0_1136:
	s_mov_b64 s[6:7], exec
	v_mbcnt_lo_u32_b32 v3, s6, 0
	v_mbcnt_hi_u32_b32 v3, s7, v3
	v_cmp_eq_u32_e32 vcc, 0, v3
	s_and_saveexec_b64 s[4:5], vcc
	s_cbranch_execz .LBB0_1138
	v_readlane_b32 s8, v255, 11
	s_lshl_b32 s8, s8, 8
	v_readlane_b32 s10, v255, 9
	v_readlane_b32 s11, v255, 10
	s_add_u32 s8, s10, s8
	s_addc_u32 s9, s11, 0
	s_bcnt1_i32_b64 s6, s[6:7]
	buffer_wbl2 sc1
	s_waitcnt vmcnt(0)
	v_mov_b32_e32 v5, 0x1000
	v_mov_b32_e32 v6, s6
	global_atomic_add v5, v5, v6, s[8:9] offset:1024 sc0

.LBB0_1152:
	s_andn2_saveexec_b64 s[4:5], s[4:5]
	s_cbranch_execz .LBB0_1170
	s_mov_b64 s[4:5], exec
	s_waitcnt lgkmcnt(0)
	s_waitcnt vmcnt(0)
	v_mbcnt_lo_u32_b32 v3, s4, 0
	v_mbcnt_hi_u32_b32 v3, s5, v3
	v_cmp_eq_u32_e32 vcc, 0, v3
	s_and_saveexec_b64 s[6:7], vcc
	s_cbranch_execz .LBB0_1155
	s_bcnt1_i32_b64 s4, s[4:5]
	v_mov_b32_e32 v5, s4
	v_readlane_b32 s4, v255, 9
	v_mov_b32_e32 v4, 0x3000
	v_readlane_b32 s5, v255, 10
	s_nop 4
	global_atomic_add v4, v4, v5, s[4:5] offset:1024 sc0

.LBB0_1249:
	s_mov_b64 s[6:7], exec
	v_mbcnt_lo_u32_b32 v3, s6, 0
	v_mbcnt_hi_u32_b32 v3, s7, v3
	v_cmp_eq_u32_e32 vcc, 0, v3
	s_and_saveexec_b64 s[2:3], vcc
	s_cbranch_execz .LBB0_1251
	v_readlane_b32 s8, v255, 11
	s_lshl_b32 s8, s8, 8
	v_readlane_b32 s12, v255, 9
	v_readlane_b32 s13, v255, 10
	s_add_u32 s8, s12, s8
	s_addc_u32 s9, s13, 0
	s_bcnt1_i32_b64 s6, s[6:7]
	buffer_wbl2 sc1
	s_waitcnt vmcnt(0)
	v_mov_b32_e32 v5, 0x1000
	v_mov_b32_e32 v6, s6
	global_atomic_add v5, v5, v6, s[8:9] offset:1024 sc0

.LBB0_1358:
	s_mov_b64 s[6:7], exec
	v_mbcnt_lo_u32_b32 v1, s6, 0
	v_mbcnt_hi_u32_b32 v1, s7, v1
	v_cmp_eq_u32_e32 vcc, 0, v1
	s_and_saveexec_b64 s[4:5], vcc
	s_cbranch_execz .LBB0_1360
	v_readlane_b32 s8, v255, 11
	s_lshl_b32 s8, s8, 8
	v_readlane_b32 s10, v255, 9
	v_readlane_b32 s11, v255, 10
	s_add_u32 s8, s10, s8
	s_addc_u32 s9, s11, 0
	s_bcnt1_i32_b64 s6, s[6:7]
	buffer_wbl2 sc1
	s_waitcnt vmcnt(0)
	v_mov_b32_e32 v3, 0x1000
	v_mov_b32_e32 v4, s6
	global_atomic_add v3, v3, v4, s[8:9] offset:1024 sc0

.LBB0_1374:
	s_andn2_saveexec_b64 s[4:5], s[4:5]
	s_cbranch_execz .LBB0_1392
	s_mov_b64 s[4:5], exec
	s_waitcnt lgkmcnt(0)
	s_waitcnt vmcnt(0)
	v_mbcnt_lo_u32_b32 v1, s4, 0
	v_mbcnt_hi_u32_b32 v1, s5, v1
	v_cmp_eq_u32_e32 vcc, 0, v1
	s_and_saveexec_b64 s[6:7], vcc
	s_cbranch_execz .LBB0_1377
	s_bcnt1_i32_b64 s4, s[4:5]
	v_mov_b32_e32 v3, s4
	v_readlane_b32 s4, v255, 9
	v_mov_b32_e32 v2, 0x3000
	v_readlane_b32 s5, v255, 10
	s_nop 4
	global_atomic_add v2, v2, v3, s[4:5] offset:1024 sc0
